# v32
# speedup vs baseline: 1.0134x; 1.0029x over previous
.LBB1_18:
	s_andn2_b64 vcc, exec, s[50:51]
	s_cbranch_vccnz .LBB1_20
	s_add_i32 m0, s43, 0x20000
	s_nop 0
	global_load_lds_dwordx4 v230, s[88:89] nt
	s_waitcnt vmcnt(9)
